# norm2: workgroup-to-row-block mapping permuted so each workgroup normalises rows whose gemm_out tiles were produced on its own XCD (L2-local reads of xb); speed only
# baseline (speedup 1.0000x reference)
.LBB0_1047:
	s_or_b64 exec, exec, s[0:1]
	s_mov_b64 s[12:13], s[72:73]
	v_mov_b32_e32 v18, v0
	s_waitcnt lgkmcnt(0)
	s_barrier
	s_nop 0
	s_mov_b64 s[14:15], exec
	s_mov_b64 s[94:95], 0x40000
	s_load_dwordx2 s[4:5], s[12:13], 0x178
	s_load_dwordx2 s[6:7], s[12:13], 0x130
	s_load_dwordx2 s[8:9], s[12:13], 0x228
	s_load_dwordx2 s[10:11], s[12:13], 0x120
	s_load_dwordx2 s[32:33], s[12:13], 0x38
	s_load_dwordx2 s[34:35], s[12:13], 0xf0
	s_load_dwordx2 s[0:1], s[12:13], 0xe8
	v_readlane_b32 s20, v255, 12
	v_readlane_b32 s36, v255, 6
	v_readlane_b32 s37, v255, 7
	v_and_b32_e32 v229, 63, v18
	v_lshlrev_b32_e32 v230, 3, v229
	v_lshlrev_b32_e32 v231, 4, v229
	v_bfe_u32 v232, v18, 2, 4
	v_lshlrev_b32_e32 v232, 2, v232
	v_and_b32_e32 v233, 8, v18
	v_cmp_eq_u32_e64 s[26:27], 0, v233
	v_and_b32_e32 v233, 4, v18
	v_cmp_eq_u32_e64 s[28:29], 0, v233
	v_and_b32_e32 v233, 3, v18
	v_cmp_eq_u32_e64 s[30:31], 0, v233
	v_mov_b32_e32 v234, 0x358637bd
	v_lshlrev_b32_e32 v220, 4, v18
	v_and_b32_e32 v221, 15, v18
	v_lshrrev_b32_e32 v222, 4, v18
	v_lshlrev_b32_e32 v221, 10, v221
	v_lshl_or_b32 v221, v222, 4, v221
	v_lshrrev_b32_e32 v222, 6, v18
	s_nop 0
	v_readfirstlane_b32 s18, v222
	s_and_b32 s19, s2, 7
	s_lshl_b32 s19, s19, 5
	s_lshr_b32 s23, s2, 3
	s_or_b32 s19, s19, s23
	s_lshl_b32 s19, s19, 3
	s_add_i32 s18, s18, s19
	s_add_i32 s19, s24, 0x7ff
	s_lshr_b32 s19, s19, 11
	s_mul_i32 s18, s18, s19
	s_add_i32 s19, s18, s19
	s_min_i32 s19, s19, s24
	s_mov_b32 s25, 0xffff0000
	s_mul_i32 s16, s20, 9
	s_mov_b32 s17, 0
	s_movk_i32 s22, 0x6000
	s_mul_i32 s21, s16, s22
	s_waitcnt lgkmcnt(0)
	s_add_u32 s0, s0, s36
	s_addc_u32 s1, s1, s37
	global_load_dwordx4 v[116:119], v220, s[0:1]
	s_add_u32 s0, s0, 0x2000
	s_addc_u32 s1, s1, 0
	global_load_dwordx4 v[120:123], v220, s[0:1]
	s_add_u32 s0, s0, 0x2000
	s_addc_u32 s1, s1, 0
	global_load_dwordx4 v[124:127], v220, s[0:1]
	s_add_u32 s0, s0, 0x2000
	s_addc_u32 s1, s1, 0
	global_load_dwordx4 v[128:131], v220, s[0:1]
	s_add_u32 s0, s0, 0x2000
	s_addc_u32 s1, s1, 0
	global_load_dwordx4 v[132:135], v220, s[0:1]
	s_add_u32 s0, s0, 0x2000
	s_addc_u32 s1, s1, 0
	global_load_dwordx4 v[136:139], v220, s[0:1]
	s_add_u32 s0, s0, 0x2000
	s_addc_u32 s1, s1, 0
	global_load_dwordx4 v[140:143], v220, s[0:1]
	s_add_u32 s0, s0, 0x2000
	s_addc_u32 s1, s1, 0
	global_load_dwordx4 v[144:147], v220, s[0:1]
	s_cmp_lt_i32 s18, s19
	s_cbranch_scc0 .Ln2_idle
	s_lshl_b32 s0, s20, 12
	s_lshl_b32 s1, s20, 6
	s_lshl_b32 s23, s18, 11
	s_lshl_b32 s36, s18, 6
	s_add_u32 s10, s10, s21
	s_addc_u32 s11, s11, 0
	s_add_u32 s32, s32, s0
	s_addc_u32 s33, s33, 0
	s_add_u32 s34, s34, s1
	s_addc_u32 s35, s35, 0
	s_add_u32 s4, s4, s23
	s_addc_u32 s5, s5, 0
	s_add_u32 s6, s6, s23
	s_addc_u32 s7, s7, 0
	s_add_u32 s8, s8, s36
	s_addc_u32 s9, s9, 0
	global_load_dwordx4 v[172:175], v231, s[32:33] offset:0
	global_load_dwordx4 v[176:179], v231, s[32:33] offset:1024
	global_load_dwordx4 v[180:183], v231, s[32:33] offset:2048
	global_load_dwordx4 v[184:187], v231, s[32:33] offset:3072
	global_load_dword v235, v232, s[34:35]
	s_add_i32 s23, s18, 1
	s_cmp_lt_i32 s23, s19
	s_cselect_b32 s21, 1, 0
	s_bitcmp0_b32 s18, 0
	s_cselect_b32 s21, s21, 0
	s_lshl_b32 s23, s21, 11
	s_lshl_b32 s36, s21, 6
	v_add_u32_e32 v236, s23, v230
	v_add_u32_e32 v238, s23, v230
	v_add_u32_e32 v237, s36, v232
	global_load_dwordx2 v[2:3], v230, s[4:5] offset:0
	global_load_dwordx2 v[4:5], v230, s[4:5] offset:512
	global_load_dwordx2 v[6:7], v230, s[4:5] offset:1024
	global_load_dwordx2 v[8:9], v230, s[4:5] offset:1536
	global_load_dwordx2 v[10:11], v236, s[4:5] offset:0
	global_load_dwordx2 v[12:13], v236, s[4:5] offset:512
	global_load_dwordx2 v[14:15], v236, s[4:5] offset:1024
	global_load_dwordx2 v[16:17], v236, s[4:5] offset:1536
	s_lshr_b32 s23, s18, 12
	s_cmp_lt_i32 s18, 0x8000
	s_cselect_b32 s20, s23, 8
	s_mul_i32 s0, s20, s22
	s_add_u32 s0, s10, s0
	s_addc_u32 s1, s11, 0
	s_add_u32 s0, s0, 0x3000
	s_addc_u32 s1, s1, 0
	global_load_dwordx4 v[68:71], v231, s[0:1] offset:0
	global_load_dwordx4 v[72:75], v231, s[0:1] offset:1024
	global_load_dwordx4 v[76:79], v231, s[0:1] offset:2048
	global_load_dwordx4 v[80:83], v231, s[0:1] offset:3072
	s_add_u32 s0, s0, 0x1000
	s_addc_u32 s1, s1, 0
	global_load_dwordx4 v[52:55], v231, s[0:1] offset:0
	global_load_dwordx4 v[56:59], v231, s[0:1] offset:1024
	global_load_dwordx4 v[60:63], v231, s[0:1] offset:2048
	global_load_dwordx4 v[64:67], v231, s[0:1] offset:3072
	s_waitcnt vmcnt(28)
	ds_write_b128 v221, v[116:119] offset:0
	s_waitcnt vmcnt(27)
	ds_write_b128 v221, v[120:123] offset:512
	s_waitcnt vmcnt(26)
	ds_write_b128 v221, v[124:127] offset:16384
	s_waitcnt vmcnt(25)
	ds_write_b128 v221, v[128:131] offset:16896
	s_waitcnt vmcnt(24)
	ds_write_b128 v221, v[132:135] offset:32768
	s_waitcnt vmcnt(23)
	ds_write_b128 v221, v[136:139] offset:33280
	s_waitcnt vmcnt(22)
	ds_write_b128 v221, v[140:143] offset:49152
	s_waitcnt vmcnt(21)
	ds_write_b128 v221, v[144:147] offset:49664
	s_waitcnt vmcnt(0) lgkmcnt(0)
	s_barrier
	v_add_f32_e32 v52, 1.0, v52
	v_add_f32_e32 v53, 1.0, v53
	v_add_f32_e32 v54, 1.0, v54
	v_add_f32_e32 v55, 1.0, v55
	v_add_f32_e32 v56, 1.0, v56
	v_add_f32_e32 v57, 1.0, v57
	v_add_f32_e32 v58, 1.0, v58
	v_add_f32_e32 v59, 1.0, v59
	v_add_f32_e32 v60, 1.0, v60
	v_add_f32_e32 v61, 1.0, v61
	v_add_f32_e32 v62, 1.0, v62
	v_add_f32_e32 v63, 1.0, v63
	v_add_f32_e32 v64, 1.0, v64
	v_add_f32_e32 v65, 1.0, v65
	v_add_f32_e32 v66, 1.0, v66
	v_add_f32_e32 v67, 1.0, v67
	v_mul_f32_e32 v52, v172, v52
	v_mul_f32_e32 v53, v173, v53
	v_mul_f32_e32 v54, v174, v54
	v_mul_f32_e32 v55, v175, v55
	v_mul_f32_e32 v56, v176, v56
	v_mul_f32_e32 v57, v177, v57
	v_mul_f32_e32 v58, v178, v58
	v_mul_f32_e32 v59, v179, v59
	v_mul_f32_e32 v60, v180, v60
	v_mul_f32_e32 v61, v181, v61
	v_mul_f32_e32 v62, v182, v62
	v_mul_f32_e32 v63, v183, v63
	v_mul_f32_e32 v64, v184, v64
	v_mul_f32_e32 v65, v185, v65
	v_mul_f32_e32 v66, v186, v66
	v_mul_f32_e32 v67, v187, v67
	s_branch .Ln2_loop
